# P8 gate/up epilogue: pairs of dwordx2 stores merged into dwordx4 with v_permlane16_swap (on top of P9 LDS-staged epilogue)
# baseline (speedup 1.0000x reference)
.LBB0_899:
	s_lshl_b32 s3, s42, 7
	s_and_b32 s3, s3, 0x380
	v_or_b32_e32 v2, s3, v213
	s_lshl_b32 s74, s69, 18
	s_add_i32 s74, s74, s3
	s_add_u32 s74, s14, s74
	s_addc_u32 s75, s15, 0
	s_lshl_b32 s3, s68, 10
	s_and_b32 s3, s3, 0x400
	s_nop 15
	s_nop 15
	v_add_u32_e32 v4, s3, v209
	ds_read_b128 v[16:19], v4
	ds_read_b128 v[12:15], v4 offset:16
	ds_read_b128 v[8:11], v4 offset:512
	ds_read_b128 v[4:7], v4 offset:528
	v_lshlrev_b32_e32 v52, 10, v225
	v_add_u32_e32 v52, v52, v213
	v_and_b32_e32 v53, 8, v213
	v_mul_u32_u24_e32 v53, 0x7ff, v53
	v_add_u32_e32 v52, v52, v53
	v_lshl_add_u32 v24, s69, 8, v225
	s_waitcnt lgkmcnt(0)
	v_pk_add_f32 v[20:21], v[82:83], v[18:19]
	v_pk_add_f32 v[26:27], v[80:81], v[16:17]
	v_pk_add_f32 v[34:35], v[144:145], v[8:9]
	v_min_f32_e32 v26, 0x40e00000, v26
	v_min_f32_e32 v27, 0x40e00000, v27
	v_med3_f32 v34, v34, s30, v252
	v_med3_f32 v35, v35, s30, v252
	v_min_f32_e32 v20, 0x40e00000, v20
	v_min_f32_e32 v21, 0x40e00000, v21
	v_pk_mul_f32 v[38:39], v[26:27], s[86:87] op_sel_hi:[1,0]
	v_pk_fma_f32 v[26:27], v[26:27], v[34:35], v[26:27]
	v_pk_mul_f32 v[34:35], v[20:21], s[86:87] op_sel_hi:[1,0]
	v_pk_add_f32 v[30:31], v[88:89], v[12:13]
	v_exp_f32_e32 v34, v34
	v_exp_f32_e32 v35, v35
	v_pk_add_f32 v[32:33], v[146:147], v[10:11]
	v_min_f32_e32 v30, 0x40e00000, v30
	v_med3_f32 v32, v32, s30, v252
	v_pk_add_f32 v[34:35], v[34:35], 1.0 op_sel_hi:[1,0]
	v_med3_f32 v33, v33, s30, v252
	v_rcp_f32_e32 v34, v34
	v_rcp_f32_e32 v35, v35
	v_min_f32_e32 v31, 0x40e00000, v31
	v_pk_fma_f32 v[20:21], v[20:21], v[32:33], v[20:21]
	v_pk_mul_f32 v[32:33], v[30:31], s[86:87] op_sel_hi:[1,0]
	v_exp_f32_e32 v38, v38
	v_exp_f32_e32 v39, v39
	v_exp_f32_e32 v32, v32
	v_exp_f32_e32 v33, v33
	v_pk_add_f32 v[28:29], v[90:91], v[14:15]
	v_pk_add_f32 v[40:41], v[154:155], v[4:5]
	v_pk_mul_f32 v[20:21], v[20:21], v[34:35]
	v_med3_f32 v34, v40, s30, v252
	v_med3_f32 v35, v41, s30, v252
	v_min_f32_e32 v28, 0x40e00000, v28
	v_min_f32_e32 v29, 0x40e00000, v29
	v_pk_fma_f32 v[30:31], v[30:31], v[34:35], v[30:31]
	v_pk_mul_f32 v[34:35], v[28:29], s[86:87] op_sel_hi:[1,0]
	v_pk_add_f32 v[38:39], v[38:39], 1.0 op_sel_hi:[1,0]
	v_pk_add_f32 v[32:33], v[32:33], 1.0 op_sel_hi:[1,0]
	v_exp_f32_e32 v34, v34
	v_exp_f32_e32 v35, v35
	v_rcp_f32_e32 v38, v38
	v_rcp_f32_e32 v39, v39
	v_rcp_f32_e32 v32, v32
	v_rcp_f32_e32 v33, v33
	v_pk_add_f32 v[36:37], v[156:157], v[6:7]
	v_pk_add_f32 v[34:35], v[34:35], 1.0 op_sel_hi:[1,0]
	v_pk_mul_f32 v[26:27], v[26:27], v[38:39]
	v_pk_mul_f32 v[30:31], v[30:31], v[32:33]
	v_med3_f32 v32, v36, s30, v252
	v_med3_f32 v33, v37, s30, v252
	v_rcp_f32_e32 v34, v34
	v_rcp_f32_e32 v35, v35
	v_mov_b32_e32 v36, v3
	v_mov_b32_e32 v37, v3
	v_cvt_pk_fp8_f32 v36, v26, v27
	v_cvt_pk_fp8_f32 v37, v30, v31
	v_pk_fma_f32 v[26:27], v[28:29], v[32:33], v[28:29]
	v_pk_add_f32 v[28:29], v[98:99], v[18:19]
	v_pk_add_f32 v[30:31], v[96:97], v[16:17]
	v_pk_add_f32 v[38:39], v[158:159], v[8:9]
	v_min_f32_e32 v30, 0x40e00000, v30
	v_min_f32_e32 v31, 0x40e00000, v31
	v_med3_f32 v38, v38, s30, v252
	v_med3_f32 v39, v39, s30, v252
	v_min_f32_e32 v28, 0x40e00000, v28
	v_min_f32_e32 v29, 0x40e00000, v29
	v_pk_mul_f32 v[26:27], v[26:27], v[34:35]
	v_pk_mul_f32 v[42:43], v[30:31], s[86:87] op_sel_hi:[1,0]
	v_pk_fma_f32 v[30:31], v[30:31], v[38:39], v[30:31]
	v_pk_mul_f32 v[38:39], v[28:29], s[86:87] op_sel_hi:[1,0]
	v_cvt_pk_fp8_f32 v36, v20, v21 op_sel:[0,0,1]
	v_cvt_pk_fp8_f32 v37, v26, v27 op_sel:[0,0,1]
	v_exp_f32_e32 v38, v38
	v_exp_f32_e32 v39, v39
	v_ashrrev_i32_e32 v25, 31, v24
	v_lshl_add_u64 v[22:23], s[14:15], 0, v[2:3]
	v_lshlrev_b64 v[20:21], 10, v[24:25]
	v_lshl_add_u64 v[20:21], v[22:23], 0, v[20:21]
	v_mov_b32_e32 v48, v36
	v_mov_b32_e32 v49, v37
	v_pk_add_f32 v[34:35], v[104:105], v[12:13]
	v_pk_add_f32 v[36:37], v[160:161], v[10:11]
	v_pk_add_f32 v[38:39], v[38:39], 1.0 op_sel_hi:[1,0]
	v_med3_f32 v36, v36, s30, v252
	v_med3_f32 v37, v37, s30, v252
	v_rcp_f32_e32 v38, v38
	v_rcp_f32_e32 v39, v39
	v_min_f32_e32 v34, 0x40e00000, v34
	v_min_f32_e32 v35, 0x40e00000, v35
	v_pk_fma_f32 v[28:29], v[28:29], v[36:37], v[28:29]
	v_pk_mul_f32 v[36:37], v[34:35], s[86:87] op_sel_hi:[1,0]
	v_exp_f32_e32 v42, v42
	v_exp_f32_e32 v43, v43
	v_exp_f32_e32 v36, v36
	v_exp_f32_e32 v37, v37
	v_pk_add_f32 v[32:33], v[106:107], v[14:15]
	v_pk_add_f32 v[44:45], v[162:163], v[4:5]
	v_pk_mul_f32 v[28:29], v[28:29], v[38:39]
	v_med3_f32 v38, v44, s30, v252
	v_med3_f32 v39, v45, s30, v252
	v_min_f32_e32 v32, 0x40e00000, v32
	v_min_f32_e32 v33, 0x40e00000, v33
	v_pk_fma_f32 v[34:35], v[34:35], v[38:39], v[34:35]
	v_pk_mul_f32 v[38:39], v[32:33], s[86:87] op_sel_hi:[1,0]
	v_pk_add_f32 v[42:43], v[42:43], 1.0 op_sel_hi:[1,0]
	v_pk_add_f32 v[36:37], v[36:37], 1.0 op_sel_hi:[1,0]
	v_exp_f32_e32 v38, v38
	v_exp_f32_e32 v39, v39
	v_rcp_f32_e32 v42, v42
	v_rcp_f32_e32 v43, v43
	v_rcp_f32_e32 v36, v36
	v_rcp_f32_e32 v37, v37
	v_pk_add_f32 v[40:41], v[164:165], v[6:7]
	v_pk_add_f32 v[38:39], v[38:39], 1.0 op_sel_hi:[1,0]
	v_pk_mul_f32 v[30:31], v[30:31], v[42:43]
	v_pk_mul_f32 v[34:35], v[34:35], v[36:37]
	v_med3_f32 v36, v40, s30, v252
	v_med3_f32 v37, v41, s30, v252
	v_rcp_f32_e32 v38, v38
	v_rcp_f32_e32 v39, v39
	v_mov_b32_e32 v40, v3
	v_mov_b32_e32 v41, v3
	v_cvt_pk_fp8_f32 v40, v30, v31
	v_cvt_pk_fp8_f32 v41, v34, v35
	v_pk_fma_f32 v[30:31], v[32:33], v[36:37], v[32:33]
	v_pk_add_f32 v[34:35], v[120:121], v[12:13]
	v_pk_mul_f32 v[30:31], v[30:31], v[38:39]
	v_cvt_pk_fp8_f32 v40, v28, v29 op_sel:[0,0,1]
	v_cvt_pk_fp8_f32 v41, v30, v31 op_sel:[0,0,1]
	v_pk_add_f32 v[28:29], v[114:115], v[18:19]
	v_pk_add_f32 v[30:31], v[112:113], v[16:17]
	v_pk_add_f32 v[38:39], v[166:167], v[8:9]
	v_min_f32_e32 v30, 0x40e00000, v30
	v_min_f32_e32 v31, 0x40e00000, v31
	v_med3_f32 v38, v38, s30, v252
	v_med3_f32 v39, v39, s30, v252
	v_min_f32_e32 v28, 0x40e00000, v28
	v_min_f32_e32 v29, 0x40e00000, v29
	v_pk_mul_f32 v[42:43], v[30:31], s[86:87] op_sel_hi:[1,0]
	v_pk_fma_f32 v[30:31], v[30:31], v[38:39], v[30:31]
	v_pk_mul_f32 v[38:39], v[28:29], s[86:87] op_sel_hi:[1,0]
	v_pk_add_f32 v[36:37], v[168:169], v[10:11]
	v_exp_f32_e32 v38, v38
	v_exp_f32_e32 v39, v39
	v_med3_f32 v36, v36, s30, v252
	v_med3_f32 v37, v37, s30, v252
	v_min_f32_e32 v34, 0x40e00000, v34
	v_pk_add_f32 v[38:39], v[38:39], 1.0 op_sel_hi:[1,0]
	v_min_f32_e32 v35, 0x40e00000, v35
	v_rcp_f32_e32 v38, v38
	v_rcp_f32_e32 v39, v39
	v_pk_fma_f32 v[28:29], v[28:29], v[36:37], v[28:29]
	v_pk_mul_f32 v[36:37], v[34:35], s[86:87] op_sel_hi:[1,0]
	v_exp_f32_e32 v42, v42
	v_exp_f32_e32 v43, v43
	v_exp_f32_e32 v36, v36
	v_exp_f32_e32 v37, v37
	v_pk_add_f32 v[32:33], v[122:123], v[14:15]
	v_pk_add_f32 v[44:45], v[170:171], v[4:5]
	v_pk_mul_f32 v[28:29], v[28:29], v[38:39]
	v_med3_f32 v38, v44, s30, v252
	v_med3_f32 v39, v45, s30, v252
	v_min_f32_e32 v32, 0x40e00000, v32
	v_min_f32_e32 v33, 0x40e00000, v33
	v_pk_fma_f32 v[34:35], v[34:35], v[38:39], v[34:35]
	v_pk_mul_f32 v[38:39], v[32:33], s[86:87] op_sel_hi:[1,0]
	v_or_b32_e32 v26, 16, v24
	v_pk_add_f32 v[42:43], v[42:43], 1.0 op_sel_hi:[1,0]
	v_pk_add_f32 v[36:37], v[36:37], 1.0 op_sel_hi:[1,0]
	v_exp_f32_e32 v38, v38
	v_exp_f32_e32 v39, v39
	v_ashrrev_i32_e32 v27, 31, v26
	v_rcp_f32_e32 v42, v42
	v_rcp_f32_e32 v43, v43
	v_rcp_f32_e32 v36, v36
	v_rcp_f32_e32 v37, v37
	v_lshlrev_b64 v[26:27], 10, v[26:27]
	v_lshl_add_u64 v[26:27], v[22:23], 0, v[26:27]
	v_mov_b32_e32 v50, v40
	v_mov_b32_e32 v51, v41
	s_nop 1
	v_permlane16_swap_b32_e32 v48, v50
	v_permlane16_swap_b32_e32 v49, v51
	global_store_dwordx4 v52, v[48:51], s[74:75]
	s_add_u32 s74, s74, 0x8000
	s_addc_u32 s75, s75, 0
	v_pk_add_f32 v[40:41], v[172:173], v[6:7]
	v_pk_add_f32 v[38:39], v[38:39], 1.0 op_sel_hi:[1,0]
	v_pk_mul_f32 v[30:31], v[30:31], v[42:43]
	v_pk_mul_f32 v[34:35], v[34:35], v[36:37]
	v_med3_f32 v36, v40, s30, v252
	v_med3_f32 v37, v41, s30, v252
	v_rcp_f32_e32 v38, v38
	v_rcp_f32_e32 v39, v39
	v_mov_b32_e32 v40, v3
	v_mov_b32_e32 v41, v3
	v_cvt_pk_fp8_f32 v40, v30, v31
	v_cvt_pk_fp8_f32 v41, v34, v35
	v_pk_fma_f32 v[30:31], v[32:33], v[36:37], v[32:33]
	v_or_b32_e32 v26, 32, v24
	v_pk_mul_f32 v[30:31], v[30:31], v[38:39]
	v_cvt_pk_fp8_f32 v40, v28, v29 op_sel:[0,0,1]
	v_cvt_pk_fp8_f32 v41, v30, v31 op_sel:[0,0,1]
	v_ashrrev_i32_e32 v27, 31, v26
	v_lshlrev_b64 v[26:27], 10, v[26:27]
	v_lshl_add_u64 v[26:27], v[22:23], 0, v[26:27]
	v_mov_b32_e32 v56, v40
	v_mov_b32_e32 v57, v41
	v_pk_add_f32 v[26:27], v[130:131], v[18:19]
	v_pk_add_f32 v[28:29], v[128:129], v[16:17]
	v_pk_add_f32 v[36:37], v[174:175], v[8:9]
	v_min_f32_e32 v28, 0x40e00000, v28
	v_min_f32_e32 v29, 0x40e00000, v29
	v_med3_f32 v36, v36, s30, v252
	v_med3_f32 v37, v37, s30, v252
	v_min_f32_e32 v26, 0x40e00000, v26
	v_min_f32_e32 v27, 0x40e00000, v27
	v_pk_mul_f32 v[40:41], v[28:29], s[86:87] op_sel_hi:[1,0]
	v_pk_fma_f32 v[28:29], v[28:29], v[36:37], v[28:29]
	v_pk_mul_f32 v[36:37], v[26:27], s[86:87] op_sel_hi:[1,0]
	v_pk_add_f32 v[32:33], v[132:133], v[12:13]
	v_exp_f32_e32 v36, v36
	v_exp_f32_e32 v37, v37
	v_pk_add_f32 v[34:35], v[176:177], v[10:11]
	v_min_f32_e32 v32, 0x40e00000, v32
	v_med3_f32 v34, v34, s30, v252
	v_pk_add_f32 v[36:37], v[36:37], 1.0 op_sel_hi:[1,0]
	v_med3_f32 v35, v35, s30, v252
	v_rcp_f32_e32 v36, v36
	v_rcp_f32_e32 v37, v37
	v_min_f32_e32 v33, 0x40e00000, v33
	v_pk_fma_f32 v[26:27], v[26:27], v[34:35], v[26:27]
	v_pk_mul_f32 v[34:35], v[32:33], s[86:87] op_sel_hi:[1,0]
	v_exp_f32_e32 v40, v40
	v_exp_f32_e32 v41, v41
	v_exp_f32_e32 v34, v34
	v_exp_f32_e32 v35, v35
	v_pk_add_f32 v[30:31], v[134:135], v[14:15]
	v_pk_add_f32 v[42:43], v[182:183], v[4:5]
	v_pk_mul_f32 v[26:27], v[26:27], v[36:37]
	v_med3_f32 v36, v42, s30, v252
	v_med3_f32 v37, v43, s30, v252
	v_min_f32_e32 v30, 0x40e00000, v30
	v_min_f32_e32 v31, 0x40e00000, v31
	v_pk_fma_f32 v[32:33], v[32:33], v[36:37], v[32:33]
	v_pk_mul_f32 v[36:37], v[30:31], s[86:87] op_sel_hi:[1,0]
	v_pk_add_f32 v[40:41], v[40:41], 1.0 op_sel_hi:[1,0]
	v_pk_add_f32 v[34:35], v[34:35], 1.0 op_sel_hi:[1,0]
	v_exp_f32_e32 v36, v36
	v_exp_f32_e32 v37, v37
	v_rcp_f32_e32 v40, v40
	v_rcp_f32_e32 v41, v41
	v_rcp_f32_e32 v34, v34
	v_rcp_f32_e32 v35, v35
	v_pk_add_f32 v[38:39], v[184:185], v[6:7]
	v_pk_add_f32 v[36:37], v[36:37], 1.0 op_sel_hi:[1,0]
	v_pk_mul_f32 v[28:29], v[28:29], v[40:41]
	v_pk_mul_f32 v[32:33], v[32:33], v[34:35]
	v_med3_f32 v34, v38, s30, v252
	v_med3_f32 v35, v39, s30, v252
	v_rcp_f32_e32 v36, v36
	v_rcp_f32_e32 v37, v37
	v_mov_b32_e32 v38, v3
	v_mov_b32_e32 v39, v3
	v_cvt_pk_fp8_f32 v38, v28, v29
	v_cvt_pk_fp8_f32 v39, v32, v33
	v_pk_fma_f32 v[28:29], v[30:31], v[34:35], v[30:31]
	v_or_b32_e32 v24, 48, v24
	v_pk_mul_f32 v[28:29], v[28:29], v[36:37]
	v_cvt_pk_fp8_f32 v38, v26, v27 op_sel:[0,0,1]
	v_cvt_pk_fp8_f32 v39, v28, v29 op_sel:[0,0,1]
	v_ashrrev_i32_e32 v25, 31, v24
	v_lshlrev_b64 v[24:25], 10, v[24:25]
	v_lshl_add_u64 v[22:23], v[22:23], 0, v[24:25]
	v_mov_b32_e32 v58, v38
	v_mov_b32_e32 v59, v39
	s_nop 1
	v_permlane16_swap_b32_e32 v56, v58
	v_permlane16_swap_b32_e32 v57, v59
	global_store_dwordx4 v52, v[56:59], s[74:75]
	s_add_u32 s74, s74, 0x18000
	s_addc_u32 s75, s75, 0
	v_pk_add_f32 v[22:23], v[70:71], v[18:19]
	v_pk_add_f32 v[24:25], v[68:69], v[16:17]
	v_pk_add_f32 v[32:33], v[124:125], v[8:9]
	v_min_f32_e32 v24, 0x40e00000, v24
	v_min_f32_e32 v25, 0x40e00000, v25
	v_med3_f32 v32, v32, s30, v252
	v_med3_f32 v33, v33, s30, v252
	v_min_f32_e32 v22, 0x40e00000, v22
	v_min_f32_e32 v23, 0x40e00000, v23
	v_pk_mul_f32 v[36:37], v[24:25], s[86:87] op_sel_hi:[1,0]
	v_pk_fma_f32 v[24:25], v[24:25], v[32:33], v[24:25]
	v_pk_mul_f32 v[32:33], v[22:23], s[86:87] op_sel_hi:[1,0]
	v_pk_add_f32 v[28:29], v[72:73], v[12:13]
	v_exp_f32_e32 v32, v32
	v_exp_f32_e32 v33, v33
	v_pk_add_f32 v[30:31], v[126:127], v[10:11]
	v_min_f32_e32 v28, 0x40e00000, v28
	v_med3_f32 v30, v30, s30, v252
	v_pk_add_f32 v[32:33], v[32:33], 1.0 op_sel_hi:[1,0]
	v_med3_f32 v31, v31, s30, v252
	v_rcp_f32_e32 v32, v32
	v_rcp_f32_e32 v33, v33
	v_min_f32_e32 v29, 0x40e00000, v29
	v_pk_fma_f32 v[22:23], v[22:23], v[30:31], v[22:23]
	v_pk_mul_f32 v[30:31], v[28:29], s[86:87] op_sel_hi:[1,0]
	v_exp_f32_e32 v36, v36
	v_exp_f32_e32 v37, v37
	v_exp_f32_e32 v30, v30
	v_exp_f32_e32 v31, v31
	v_pk_add_f32 v[26:27], v[74:75], v[14:15]
	v_pk_add_f32 v[38:39], v[136:137], v[4:5]
	v_pk_mul_f32 v[22:23], v[22:23], v[32:33]
	v_med3_f32 v32, v38, s30, v252
	v_med3_f32 v33, v39, s30, v252
	v_min_f32_e32 v26, 0x40e00000, v26
	v_min_f32_e32 v27, 0x40e00000, v27
	v_pk_fma_f32 v[28:29], v[28:29], v[32:33], v[28:29]
	v_pk_mul_f32 v[32:33], v[26:27], s[86:87] op_sel_hi:[1,0]
	v_pk_add_f32 v[36:37], v[36:37], 1.0 op_sel_hi:[1,0]
	v_pk_add_f32 v[30:31], v[30:31], 1.0 op_sel_hi:[1,0]
	v_exp_f32_e32 v32, v32
	v_exp_f32_e32 v33, v33
	v_rcp_f32_e32 v36, v36
	v_rcp_f32_e32 v37, v37
	v_rcp_f32_e32 v30, v30
	v_rcp_f32_e32 v31, v31
	v_pk_add_f32 v[34:35], v[138:139], v[6:7]
	v_pk_add_f32 v[32:33], v[32:33], 1.0 op_sel_hi:[1,0]
	v_pk_mul_f32 v[24:25], v[24:25], v[36:37]
	v_pk_mul_f32 v[28:29], v[28:29], v[30:31]
	v_med3_f32 v30, v34, s30, v252
	v_med3_f32 v31, v35, s30, v252
	v_rcp_f32_e32 v32, v32
	v_rcp_f32_e32 v33, v33
	v_mov_b32_e32 v34, v3
	v_mov_b32_e32 v35, v3
	v_cvt_pk_fp8_f32 v34, v24, v25
	v_cvt_pk_fp8_f32 v35, v28, v29
	v_pk_fma_f32 v[24:25], v[26:27], v[30:31], v[26:27]
	s_mov_b32 s3, 0x20000
	v_pk_mul_f32 v[24:25], v[24:25], v[32:33]
	v_cvt_pk_fp8_f32 v34, v22, v23 op_sel:[0,0,1]
	v_cvt_pk_fp8_f32 v35, v24, v25 op_sel:[0,0,1]
	v_add_co_u32_e32 v22, vcc, s3, v20
	v_pk_add_f32 v[24:25], v[76:77], v[16:17]
	s_nop 0
	v_addc_co_u32_e32 v23, vcc, 0, v21, vcc
	v_mov_b32_e32 v48, v34
	v_mov_b32_e32 v49, v35
	v_pk_add_f32 v[22:23], v[78:79], v[18:19]
	v_pk_add_f32 v[32:33], v[140:141], v[8:9]
	v_min_f32_e32 v24, 0x40e00000, v24
	v_min_f32_e32 v25, 0x40e00000, v25
	v_med3_f32 v32, v32, s30, v252
	v_med3_f32 v33, v33, s30, v252
	v_min_f32_e32 v22, 0x40e00000, v22
	v_min_f32_e32 v23, 0x40e00000, v23
	v_pk_mul_f32 v[36:37], v[24:25], s[86:87] op_sel_hi:[1,0]
	v_pk_fma_f32 v[24:25], v[24:25], v[32:33], v[24:25]
	v_pk_mul_f32 v[32:33], v[22:23], s[86:87] op_sel_hi:[1,0]
	v_pk_add_f32 v[28:29], v[84:85], v[12:13]
	v_exp_f32_e32 v32, v32
	v_exp_f32_e32 v33, v33
	v_pk_add_f32 v[30:31], v[142:143], v[10:11]
	v_min_f32_e32 v28, 0x40e00000, v28
	v_med3_f32 v30, v30, s30, v252
	v_pk_add_f32 v[32:33], v[32:33], 1.0 op_sel_hi:[1,0]
	v_med3_f32 v31, v31, s30, v252
	v_rcp_f32_e32 v32, v32
	v_rcp_f32_e32 v33, v33
	v_min_f32_e32 v29, 0x40e00000, v29
	v_pk_fma_f32 v[22:23], v[22:23], v[30:31], v[22:23]
	v_pk_mul_f32 v[30:31], v[28:29], s[86:87] op_sel_hi:[1,0]
	v_exp_f32_e32 v36, v36
	v_exp_f32_e32 v37, v37
	v_exp_f32_e32 v30, v30
	v_exp_f32_e32 v31, v31
	v_pk_add_f32 v[26:27], v[86:87], v[14:15]
	v_pk_add_f32 v[38:39], v[150:151], v[4:5]
	v_pk_mul_f32 v[22:23], v[22:23], v[32:33]
	v_med3_f32 v32, v38, s30, v252
	v_med3_f32 v33, v39, s30, v252
	v_min_f32_e32 v26, 0x40e00000, v26
	v_min_f32_e32 v27, 0x40e00000, v27
	v_pk_fma_f32 v[28:29], v[28:29], v[32:33], v[28:29]
	v_pk_mul_f32 v[32:33], v[26:27], s[86:87] op_sel_hi:[1,0]
	v_pk_add_f32 v[36:37], v[36:37], 1.0 op_sel_hi:[1,0]
	v_pk_add_f32 v[30:31], v[30:31], 1.0 op_sel_hi:[1,0]
	v_exp_f32_e32 v32, v32
	v_exp_f32_e32 v33, v33
	v_rcp_f32_e32 v36, v36
	v_rcp_f32_e32 v37, v37
	v_rcp_f32_e32 v30, v30
	v_rcp_f32_e32 v31, v31
	v_pk_add_f32 v[34:35], v[152:153], v[6:7]
	v_pk_add_f32 v[32:33], v[32:33], 1.0 op_sel_hi:[1,0]
	v_pk_mul_f32 v[24:25], v[24:25], v[36:37]
	v_pk_mul_f32 v[28:29], v[28:29], v[30:31]
	v_med3_f32 v30, v34, s30, v252
	v_med3_f32 v31, v35, s30, v252
	v_rcp_f32_e32 v32, v32
	v_rcp_f32_e32 v33, v33
	v_mov_b32_e32 v34, v3
	v_mov_b32_e32 v35, v3
	v_cvt_pk_fp8_f32 v34, v24, v25
	v_cvt_pk_fp8_f32 v35, v28, v29
	v_pk_fma_f32 v[24:25], v[26:27], v[30:31], v[26:27]
	s_mov_b32 s3, 0x24000
	v_pk_mul_f32 v[24:25], v[24:25], v[32:33]
	v_cvt_pk_fp8_f32 v34, v22, v23 op_sel:[0,0,1]
	v_cvt_pk_fp8_f32 v35, v24, v25 op_sel:[0,0,1]
	v_add_co_u32_e32 v22, vcc, s3, v20
	v_pk_add_f32 v[24:25], v[92:93], v[16:17]
	s_nop 0
	v_addc_co_u32_e32 v23, vcc, 0, v21, vcc
	v_mov_b32_e32 v50, v34
	v_mov_b32_e32 v51, v35
	s_nop 1
	v_permlane16_swap_b32_e32 v48, v50
	v_permlane16_swap_b32_e32 v49, v51
	global_store_dwordx4 v52, v[48:51], s[74:75]
	s_add_u32 s74, s74, 0x8000
	s_addc_u32 s75, s75, 0
	v_pk_add_f32 v[22:23], v[94:95], v[18:19]
	v_pk_add_f32 v[32:33], v[178:179], v[8:9]
	v_min_f32_e32 v24, 0x40e00000, v24
	v_min_f32_e32 v25, 0x40e00000, v25
	v_med3_f32 v32, v32, s30, v252
	v_med3_f32 v33, v33, s30, v252
	v_min_f32_e32 v22, 0x40e00000, v22
	v_min_f32_e32 v23, 0x40e00000, v23
	v_pk_mul_f32 v[36:37], v[24:25], s[86:87] op_sel_hi:[1,0]
	v_pk_fma_f32 v[24:25], v[24:25], v[32:33], v[24:25]
	v_pk_mul_f32 v[32:33], v[22:23], s[86:87] op_sel_hi:[1,0]
	v_pk_add_f32 v[28:29], v[100:101], v[12:13]
	v_exp_f32_e32 v32, v32
	v_exp_f32_e32 v33, v33
	v_pk_add_f32 v[30:31], v[180:181], v[10:11]
	v_min_f32_e32 v28, 0x40e00000, v28
	v_med3_f32 v30, v30, s30, v252
	v_pk_add_f32 v[32:33], v[32:33], 1.0 op_sel_hi:[1,0]
	v_med3_f32 v31, v31, s30, v252
	v_rcp_f32_e32 v32, v32
	v_rcp_f32_e32 v33, v33
	v_min_f32_e32 v29, 0x40e00000, v29
	v_pk_fma_f32 v[22:23], v[22:23], v[30:31], v[22:23]
	v_pk_mul_f32 v[30:31], v[28:29], s[86:87] op_sel_hi:[1,0]
	v_exp_f32_e32 v36, v36
	v_exp_f32_e32 v37, v37
	v_exp_f32_e32 v30, v30
	v_exp_f32_e32 v31, v31
	v_pk_add_f32 v[26:27], v[102:103], v[14:15]
	v_pk_add_f32 v[38:39], v[186:187], v[4:5]
	v_pk_mul_f32 v[22:23], v[22:23], v[32:33]
	v_med3_f32 v32, v38, s30, v252
	v_med3_f32 v33, v39, s30, v252
	v_min_f32_e32 v26, 0x40e00000, v26
	v_min_f32_e32 v27, 0x40e00000, v27
	v_pk_fma_f32 v[28:29], v[28:29], v[32:33], v[28:29]
	v_pk_mul_f32 v[32:33], v[26:27], s[86:87] op_sel_hi:[1,0]
	v_pk_add_f32 v[36:37], v[36:37], 1.0 op_sel_hi:[1,0]
	v_pk_add_f32 v[30:31], v[30:31], 1.0 op_sel_hi:[1,0]
	v_exp_f32_e32 v32, v32
	v_exp_f32_e32 v33, v33
	v_rcp_f32_e32 v36, v36
	v_rcp_f32_e32 v37, v37
	v_rcp_f32_e32 v30, v30
	v_rcp_f32_e32 v31, v31
	v_pk_add_f32 v[34:35], v[188:189], v[6:7]
	v_pk_add_f32 v[32:33], v[32:33], 1.0 op_sel_hi:[1,0]
	v_pk_mul_f32 v[24:25], v[24:25], v[36:37]
	v_pk_mul_f32 v[28:29], v[28:29], v[30:31]
	v_med3_f32 v30, v34, s30, v252
	v_med3_f32 v31, v35, s30, v252
	v_rcp_f32_e32 v32, v32
	v_rcp_f32_e32 v33, v33
	v_mov_b32_e32 v34, v3
	v_mov_b32_e32 v35, v3
	v_cvt_pk_fp8_f32 v34, v24, v25
	v_cvt_pk_fp8_f32 v35, v28, v29
	v_pk_fma_f32 v[24:25], v[26:27], v[30:31], v[26:27]
	s_mov_b32 s3, 0x28000
	v_pk_mul_f32 v[24:25], v[24:25], v[32:33]
	v_cvt_pk_fp8_f32 v34, v22, v23 op_sel:[0,0,1]
	v_cvt_pk_fp8_f32 v35, v24, v25 op_sel:[0,0,1]
	v_add_co_u32_e32 v22, vcc, s3, v20
	v_pk_add_f32 v[16:17], v[108:109], v[16:17]
	v_pk_add_f32 v[8:9], v[190:191], v[8:9]
	v_addc_co_u32_e32 v23, vcc, 0, v21, vcc
	v_pk_add_f32 v[18:19], v[110:111], v[18:19]
	v_pk_add_f32 v[12:13], v[116:117], v[12:13]
	v_pk_add_f32 v[10:11], v[192:193], v[10:11]
	v_min_f32_e32 v16, 0x40e00000, v16
	v_min_f32_e32 v17, 0x40e00000, v17
	v_med3_f32 v8, v8, s30, v252
	v_med3_f32 v9, v9, s30, v252
	v_mov_b32_e32 v56, v34
	v_mov_b32_e32 v57, v35
	v_pk_mul_f32 v[22:23], v[16:17], s[86:87] op_sel_hi:[1,0]
	v_pk_fma_f32 v[8:9], v[16:17], v[8:9], v[16:17]
	v_min_f32_e32 v16, 0x40e00000, v18
	v_min_f32_e32 v17, 0x40e00000, v19
	v_med3_f32 v10, v10, s30, v252
	v_med3_f32 v11, v11, s30, v252
	v_min_f32_e32 v12, 0x40e00000, v12
	v_min_f32_e32 v13, 0x40e00000, v13
	v_pk_mul_f32 v[18:19], v[16:17], s[86:87] op_sel_hi:[1,0]
	v_pk_fma_f32 v[10:11], v[16:17], v[10:11], v[16:17]
	v_pk_mul_f32 v[16:17], v[12:13], s[86:87] op_sel_hi:[1,0]
	v_exp_f32_e32 v22, v22
	v_exp_f32_e32 v23, v23
	v_pk_add_f32 v[4:5], v[194:195], v[4:5]
	v_exp_f32_e32 v16, v16
	v_exp_f32_e32 v17, v17
	v_pk_add_f32 v[14:15], v[118:119], v[14:15]
	v_med3_f32 v4, v4, s30, v252
	v_med3_f32 v5, v5, s30, v252
	v_pk_fma_f32 v[4:5], v[12:13], v[4:5], v[12:13]
	v_min_f32_e32 v12, 0x40e00000, v14
	v_min_f32_e32 v13, 0x40e00000, v15
	v_pk_mul_f32 v[14:15], v[12:13], s[86:87] op_sel_hi:[1,0]
	v_pk_add_f32 v[22:23], v[22:23], 1.0 op_sel_hi:[1,0]
	v_exp_f32_e32 v18, v18
	v_exp_f32_e32 v19, v19
	v_pk_add_f32 v[16:17], v[16:17], 1.0 op_sel_hi:[1,0]
	v_exp_f32_e32 v14, v14
	v_exp_f32_e32 v15, v15
	v_rcp_f32_e32 v22, v22
	v_rcp_f32_e32 v23, v23
	v_rcp_f32_e32 v16, v16
	v_rcp_f32_e32 v17, v17
	v_pk_add_f32 v[18:19], v[18:19], 1.0 op_sel_hi:[1,0]
	v_pk_add_f32 v[14:15], v[14:15], 1.0 op_sel_hi:[1,0]
	v_pk_mul_f32 v[8:9], v[8:9], v[22:23]
	v_rcp_f32_e32 v18, v18
	v_rcp_f32_e32 v19, v19
	v_pk_mul_f32 v[4:5], v[4:5], v[16:17]
	v_rcp_f32_e32 v14, v14
	v_rcp_f32_e32 v15, v15
	v_mov_b32_e32 v16, v3
	v_mov_b32_e32 v17, v3
	v_pk_add_f32 v[6:7], v[196:197], v[6:7]
	v_cvt_pk_fp8_f32 v16, v8, v9
	v_cvt_pk_fp8_f32 v17, v4, v5
	v_med3_f32 v6, v6, s30, v252
	v_med3_f32 v7, v7, s30, v252
	v_pk_fma_f32 v[4:5], v[12:13], v[6:7], v[12:13]
	v_pk_mul_f32 v[10:11], v[10:11], v[18:19]
	v_pk_mul_f32 v[4:5], v[4:5], v[14:15]
	v_cvt_pk_fp8_f32 v16, v10, v11 op_sel:[0,0,1]
	v_cvt_pk_fp8_f32 v17, v4, v5 op_sel:[0,0,1]
	v_add_co_u32_e32 v4, vcc, 0x2c000, v20
	s_cmp_eq_u32 s68, s65
	s_nop 0
	v_addc_co_u32_e32 v5, vcc, 0, v21, vcc
	s_mov_b64 s[40:41], -1
	v_mov_b32_e32 v58, v16
	v_mov_b32_e32 v59, v17
	s_nop 1
	v_permlane16_swap_b32_e32 v56, v58
	v_permlane16_swap_b32_e32 v57, v59
	global_store_dwordx4 v52, v[56:59], s[74:75]
	s_cbranch_scc1 .LBB0_882
	s_andn2_b64 vcc, exec, s[8:9]
	s_cbranch_vccnz .LBB0_902
	s_ashr_i32 s40, s20, 3
	s_ashr_i32 s41, s40, 31
	s_lshl_b64 s[40:41], s[40:41], 13
	s_add_u32 s3, s52, s40
	s_addc_u32 s21, s53, s41
	s_lshl_b32 s27, s20, 9
	s_and_b32 s27, s27, 0xe00
	s_add_u32 s40, s3, s27
	s_addc_u32 s41, s21, 0
	s_lshl_b32 s3, s67, 10
	v_mov_b32_e32 v203, v3
	s_and_b32 s3, s3, 0x400
	v_lshl_add_u64 v[4:5], s[40:41], 0, v[202:203]
	v_mov_b32_e32 v205, v3
	s_add_i32 s3, s3, 0
	v_lshl_add_u64 v[4:5], v[4:5], 0, v[204:205]
	s_add_i32 m0, s3, 0x24000
	s_nop 0
	global_load_lds_dwordx4 v[4:5], off
